# GLA workgroups go straight to the phase barrier when their scan is done (they used to set up the NA unit state and poll its exhausted queue first)
# baseline (speedup 1.0000x reference)
; __device__ __forceinline__ void gla_fast_unit(int unit, const bf16_t* P, const float* w_up, const float* b_up, float* Of, float* Ob, LAS unsigned char* lds0) {
;     ...
;     }
;     __syncthreads();
; }
; __global__ void __launch_bounds__(512, 2) mk_fwd(Args a) {
;     ...
;         if (bid < 64) { gla_fast_unit(bid, Pb, a.in[I_GLAWUP], a.in[I_GLABUP], Of, Ob, lds); }
;         unsigned* qctr = (unsigned*)(ws + WS_CTL) + 8192 + 64 * rep;
.LBB0_1205:
	s_waitcnt lgkmcnt(0)
	s_barrier
	v_cmp_eq_u32_e32 vcc, 0, v0
	s_and_saveexec_b64 s[6:7], vcc
	v_mov_b32_e32 v2, 0x9100
	v_mov_b32_e32 v3, 1
	global_atomic_add v2, v3, s[94:95]
	s_mov_b64 exec, s[6:7]
	s_branch .LBB0_1316
